# QKV tiles copy-out: all 8 LDS reads issued first, counted lgkmcnt per store (epilogue store ladder de-serialised)
# speedup vs baseline: 1.0177x; 1.0012x over previous
.Lqk_epi_join:
	s_ashr_i32 s5, s21, 2
	s_and_b32 s6, s6, 0x300
	v_lshlrev_b32_e32 v1, 3, v0
	v_and_b32_e32 v1, 56, v1
	s_mov_b64 s[0:1], -1
	s_waitcnt vmcnt(0) lgkmcnt(0)
	s_barrier
	s_cmp_gt_i32 s20, 15
	s_cbranch_scc1 .LBB1_105
	s_cmp_gt_i32 s20, 7
	s_cselect_b32 s1, s13, s11
	s_cselect_b32 s0, s12, s10
	s_lshl_b32 s3, s20, 11
	s_lshl_b32 s2, s5, 14
	s_and_b32 s3, s3, 0x3800
	s_or_b32 s2, s2, s3
	s_or_b32 s2, s2, s6
	v_lshrrev_b32_e32 v66, 3, v0
	v_and_b32_e32 v67, 7, v0
	v_or_b32_e32 v68, s2, v66
	v_and_b32_e32 v69, 7, v66
	v_lshlrev_b32_e32 v68, 7, v68
	v_xor_b32_e32 v69, v69, v67
	v_lshl_or_b32 v68, v67, 4, v68
	v_lshlrev_b32_e32 v69, 4, v69
	v_lshl_or_b32 v69, v66, 7, v69
	ds_read_b128 v[2:5], v69
	ds_read_b128 v[6:9], v69 offset:8192
	ds_read_b128 v[10:13], v69 offset:16384
	ds_read_b128 v[14:17], v69 offset:24576
	ds_read_b128 v[18:21], v69 offset:32768
	ds_read_b128 v[22:25], v69 offset:40960
	ds_read_b128 v[26:29], v69 offset:49152
	ds_read_b128 v[30:33], v69 offset:57344
	s_waitcnt lgkmcnt(7)
	global_store_dwordx4 v68, v[2:5], s[0:1] nt
	s_waitcnt lgkmcnt(6)
	v_add_u32_e32 v70, 0x2000, v68
	global_store_dwordx4 v70, v[6:9], s[0:1] nt
	s_waitcnt lgkmcnt(5)
	v_add_u32_e32 v70, 0x4000, v68
	global_store_dwordx4 v70, v[10:13], s[0:1] nt
	s_waitcnt lgkmcnt(4)
	v_add_u32_e32 v70, 0x6000, v68
	global_store_dwordx4 v70, v[14:17], s[0:1] nt
	s_waitcnt lgkmcnt(3)
	v_add_u32_e32 v70, 0x20000, v68
	global_store_dwordx4 v70, v[18:21], s[0:1] nt
	s_waitcnt lgkmcnt(2)
	v_add_u32_e32 v70, 0x22000, v68
	global_store_dwordx4 v70, v[22:25], s[0:1] nt
	s_waitcnt lgkmcnt(1)
	v_add_u32_e32 v70, 0x24000, v68
	global_store_dwordx4 v70, v[26:29], s[0:1] nt
	s_waitcnt lgkmcnt(0)
	v_add_u32_e32 v70, 0x26000, v68
	global_store_dwordx4 v70, v[30:33], s[0:1] nt
	s_branch .LBB1_107
.LBB1_105:
	s_lshl_b32 s2, s5, 10
	s_and_b32 s3, s4, 0x380
	s_or_b32 s2, s2, s3
	s_lshl_b32 s0, s6, 1
	s_add_u32 s0, s14, s0
	s_addc_u32 s1, s15, 0
	v_lshrrev_b32_e32 v66, 5, v0
	v_and_b32_e32 v67, 31, v0
	v_or_b32_e32 v68, s2, v66
	v_and_b32_e32 v69, 7, v66
	v_lshlrev_b32_e32 v68, 11, v68
	v_xor_b32_e32 v69, v69, v67
	v_lshl_or_b32 v68, v67, 4, v68
	v_lshlrev_b32_e32 v69, 4, v69
	v_lshl_or_b32 v69, v66, 9, v69
	ds_read_b128 v[2:5], v69
	ds_read_b128 v[6:9], v69 offset:8192
	ds_read_b128 v[10:13], v69 offset:16384
	ds_read_b128 v[14:17], v69 offset:24576
	ds_read_b128 v[18:21], v69 offset:32768
	ds_read_b128 v[22:25], v69 offset:40960
	ds_read_b128 v[26:29], v69 offset:49152
	ds_read_b128 v[30:33], v69 offset:57344
	s_waitcnt lgkmcnt(7)
	global_store_dwordx4 v68, v[2:5], s[0:1] nt
	s_waitcnt lgkmcnt(6)
	v_add_u32_e32 v70, 0x8000, v68
	global_store_dwordx4 v70, v[6:9], s[0:1] nt
	s_waitcnt lgkmcnt(5)
	v_add_u32_e32 v70, 0x10000, v68
	global_store_dwordx4 v70, v[10:13], s[0:1] nt
	s_waitcnt lgkmcnt(4)
	v_add_u32_e32 v70, 0x18000, v68
	global_store_dwordx4 v70, v[14:17], s[0:1] nt
	s_waitcnt lgkmcnt(3)
	v_add_u32_e32 v70, 0x20000, v68
	global_store_dwordx4 v70, v[18:21], s[0:1] nt
	s_waitcnt lgkmcnt(2)
	v_add_u32_e32 v70, 0x28000, v68
	global_store_dwordx4 v70, v[22:25], s[0:1] nt
	s_waitcnt lgkmcnt(1)
	v_add_u32_e32 v70, 0x30000, v68
	global_store_dwordx4 v70, v[26:29], s[0:1] nt
	s_waitcnt lgkmcnt(0)
	v_add_u32_e32 v70, 0x38000, v68
	global_store_dwordx4 v70, v[30:33], s[0:1] nt
